# s24 + P0 silu(c) fill: 20 loads in one batch (was 5 serial round trips at kernel start on the mod-GEMV workgroups)
# baseline (speedup 1.0000x reference)
; #define LBAR() do { asm volatile("s_waitcnt lgkmcnt(0)" ::: "memory"); __builtin_amdgcn_s_barrier(); asm volatile("" ::: "memory"); } while (0)
; __device__ __forceinline__ float siluf(float x) { return x / (1.0f + expf(-x)); }
; __global__ void __launch_bounds__(NTHREADS, 2) fwd(Args args) {
;     ...
;             if (bid < 192) {
;                 for (int i = tid; i < 5 * D; i += NTHREADS) { const int r = i / D, k = i % D; const float v = r < 4 ? cvec[r * D + k] : c_ctx[k]; sc[i] = siluf(v); }
;                 LBAR();
.LBB0_5:
	s_or_b64 exec, exec, s[0:1]
	v_readlane_b32 s0, v246, 10
	s_lshl_b32 s92, s0, 3
	v_readlane_b32 s1, v246, 11
	s_add_u32 s0, s88, 0x180000
	s_addc_u32 s1, s89, 0
	v_writelane_b32 v246, s0, 19
	v_and_b32_e32 v220, 63, v0
	s_nop 0
	v_writelane_b32 v246, s1, 20
	s_lshr_b32 s1, s51, 6
	s_lshl_b32 s0, s94, 3
	s_add_i32 s50, s1, s0
	s_add_u32 s96, s88, 0x100000
	s_addc_u32 s97, s89, 0
	s_add_u32 s93, s88, 0x4000000
	s_addc_u32 s0, s89, 0
	s_add_u32 s48, s88, 0x1a0000
	s_addc_u32 s49, s89, 0
	v_writelane_b32 v246, s1, 21
	s_cmp_lt_i32 s90, 1
	v_writelane_b32 v246, s0, 22
	s_cselect_b64 s[0:1], -1, 0
	s_cmp_gt_i32 s91, 0
	s_cselect_b64 s[2:3], -1, 0
	s_and_b64 s[14:15], s[0:1], s[2:3]
	s_and_b64 vcc, exec, s[14:15]
	s_cbranch_vccz .LBB0_124
	s_cmpk_lt_i32 s94, 0xc0
	s_cselect_b64 s[0:1], -1, 0
	s_cmpk_gt_i32 s94, 0xbf
	s_cbranch_scc1 .LBB0_22
	s_mov_b32 s33, 0xbfb8aa3b
	s_mov_b32 s36, 0x42ce8ed0
	s_mov_b32 s37, 0xc2b17218
	v_mov_b32_e32 v7, 0x7f800000
	global_load_dword v40, v194, s[18:19]
	v_add_u32_e32 v61, 0x800, v194
	global_load_dword v41, v61, s[18:19]
	v_add_u32_e32 v60, 0x1000, v194
	global_load_dword v42, v60, s[18:19]
	v_add_u32_e32 v61, 0x1800, v194
	global_load_dword v43, v61, s[18:19]
	v_add_u32_e32 v60, 0x2000, v194
	global_load_dword v44, v60, s[18:19]
	v_add_u32_e32 v61, 0x2800, v194
	global_load_dword v45, v61, s[18:19]
	v_add_u32_e32 v60, 0x3000, v194
	global_load_dword v46, v60, s[18:19]
	v_add_u32_e32 v61, 0x3800, v194
	global_load_dword v47, v61, s[18:19]
	v_add_u32_e32 v60, 0x4000, v194
	global_load_dword v48, v60, s[18:19]
	v_add_u32_e32 v61, 0x4800, v194
	global_load_dword v49, v61, s[18:19]
	v_add_u32_e32 v60, 0x5000, v194
	global_load_dword v50, v60, s[18:19]
	v_add_u32_e32 v61, 0x5800, v194
	global_load_dword v51, v61, s[18:19]
	v_add_u32_e32 v60, 0x6000, v194
	global_load_dword v52, v60, s[18:19]
	v_add_u32_e32 v61, 0x6800, v194
	global_load_dword v53, v61, s[18:19]
	v_add_u32_e32 v60, 0x7000, v194
	global_load_dword v54, v60, s[18:19]
	v_add_u32_e32 v61, 0x7800, v194
	global_load_dword v55, v61, s[18:19]
	global_load_dword v56, v194, s[22:23]
	v_add_u32_e32 v61, 0x800, v194
	global_load_dword v57, v61, s[22:23]
	v_add_u32_e32 v60, 0x1000, v194
	global_load_dword v58, v60, s[22:23]
	v_add_u32_e32 v61, 0x1800, v194
	global_load_dword v59, v61, s[22:23]
	s_waitcnt vmcnt(0)
	v_mul_f32_e32 v8, 0xbfb8aa3b, v40
	v_fma_f32 v9, v40, s33, -v8
	v_rndne_f32_e32 v10, v8
	v_fmac_f32_e32 v9, 0xb2a5705f, v40
	v_sub_f32_e32 v8, v8, v10
	v_add_f32_e32 v8, v8, v9
	v_cvt_i32_f32_e32 v10, v10
	v_exp_f32_e32 v8, v8
	v_cmp_nlt_f32_e32 vcc, s36, v40
	v_ldexp_f32 v8, v8, v10
	s_nop 0
	v_cndmask_b32_e32 v8, 0, v8, vcc
	v_cmp_ngt_f32_e32 vcc, s37, v40
	s_nop 1
	v_cndmask_b32_e32 v8, v7, v8, vcc
	v_add_f32_e32 v8, 1.0, v8
	v_div_scale_f32 v9, s[34:35], v8, v8, v40
	v_rcp_f32_e32 v10, v9
	v_div_scale_f32 v11, vcc, v40, v8, v40
	v_fma_f32 v12, -v9, v10, 1.0
	v_fmac_f32_e32 v10, v12, v10
	v_mul_f32_e32 v12, v11, v10
	v_fma_f32 v13, -v9, v12, v11
	v_fmac_f32_e32 v12, v13, v10
	v_fma_f32 v9, -v9, v12, v11
	v_div_fmas_f32 v9, v9, v10, v12
	v_div_fixup_f32 v40, v9, v8, v40
	ds_write_b32 v194, v40
	v_mul_f32_e32 v8, 0xbfb8aa3b, v41
	v_fma_f32 v9, v41, s33, -v8
	v_rndne_f32_e32 v10, v8
	v_fmac_f32_e32 v9, 0xb2a5705f, v41
	v_sub_f32_e32 v8, v8, v10
	v_add_f32_e32 v8, v8, v9
	v_cvt_i32_f32_e32 v10, v10
	v_exp_f32_e32 v8, v8
	v_cmp_nlt_f32_e32 vcc, s36, v41
	v_ldexp_f32 v8, v8, v10
	s_nop 0
	v_cndmask_b32_e32 v8, 0, v8, vcc
	v_cmp_ngt_f32_e32 vcc, s37, v41
	s_nop 1
	v_cndmask_b32_e32 v8, v7, v8, vcc
	v_add_f32_e32 v8, 1.0, v8
	v_div_scale_f32 v9, s[34:35], v8, v8, v41
	v_rcp_f32_e32 v10, v9
	v_div_scale_f32 v11, vcc, v41, v8, v41
	v_fma_f32 v12, -v9, v10, 1.0
	v_fmac_f32_e32 v10, v12, v10
	v_mul_f32_e32 v12, v11, v10
	v_fma_f32 v13, -v9, v12, v11
	v_fmac_f32_e32 v12, v13, v10
	v_fma_f32 v9, -v9, v12, v11
	v_div_fmas_f32 v9, v9, v10, v12
	v_div_fixup_f32 v41, v9, v8, v41
	ds_write_b32 v194, v41 offset:2048
	v_mul_f32_e32 v8, 0xbfb8aa3b, v42
	v_fma_f32 v9, v42, s33, -v8
	v_rndne_f32_e32 v10, v8
	v_fmac_f32_e32 v9, 0xb2a5705f, v42
	v_sub_f32_e32 v8, v8, v10
	v_add_f32_e32 v8, v8, v9
	v_cvt_i32_f32_e32 v10, v10
	v_exp_f32_e32 v8, v8
	v_cmp_nlt_f32_e32 vcc, s36, v42
	v_ldexp_f32 v8, v8, v10
	s_nop 0
	v_cndmask_b32_e32 v8, 0, v8, vcc
	v_cmp_ngt_f32_e32 vcc, s37, v42
	s_nop 1
	v_cndmask_b32_e32 v8, v7, v8, vcc
	v_add_f32_e32 v8, 1.0, v8
	v_div_scale_f32 v9, s[34:35], v8, v8, v42
	v_rcp_f32_e32 v10, v9
	v_div_scale_f32 v11, vcc, v42, v8, v42
	v_fma_f32 v12, -v9, v10, 1.0
	v_fmac_f32_e32 v10, v12, v10
	v_mul_f32_e32 v12, v11, v10
	v_fma_f32 v13, -v9, v12, v11
	v_fmac_f32_e32 v12, v13, v10
	v_fma_f32 v9, -v9, v12, v11
	v_div_fmas_f32 v9, v9, v10, v12
	v_div_fixup_f32 v42, v9, v8, v42
	ds_write_b32 v194, v42 offset:4096
	v_mul_f32_e32 v8, 0xbfb8aa3b, v43
	v_fma_f32 v9, v43, s33, -v8
	v_rndne_f32_e32 v10, v8
	v_fmac_f32_e32 v9, 0xb2a5705f, v43
	v_sub_f32_e32 v8, v8, v10
	v_add_f32_e32 v8, v8, v9
	v_cvt_i32_f32_e32 v10, v10
	v_exp_f32_e32 v8, v8
	v_cmp_nlt_f32_e32 vcc, s36, v43
	v_ldexp_f32 v8, v8, v10
	s_nop 0
	v_cndmask_b32_e32 v8, 0, v8, vcc
	v_cmp_ngt_f32_e32 vcc, s37, v43
	s_nop 1
	v_cndmask_b32_e32 v8, v7, v8, vcc
	v_add_f32_e32 v8, 1.0, v8
	v_div_scale_f32 v9, s[34:35], v8, v8, v43
	v_rcp_f32_e32 v10, v9
	v_div_scale_f32 v11, vcc, v43, v8, v43
	v_fma_f32 v12, -v9, v10, 1.0
	v_fmac_f32_e32 v10, v12, v10
	v_mul_f32_e32 v12, v11, v10
	v_fma_f32 v13, -v9, v12, v11
	v_fmac_f32_e32 v12, v13, v10
	v_fma_f32 v9, -v9, v12, v11
	v_div_fmas_f32 v9, v9, v10, v12
	v_div_fixup_f32 v43, v9, v8, v43
	ds_write_b32 v194, v43 offset:6144
	v_mul_f32_e32 v8, 0xbfb8aa3b, v44
; __device__ __forceinline__ float siluf(float x) { return x / (1.0f + expf(-x)); }
; __global__ void __launch_bounds__(NTHREADS, 2) fwd(Args args) {
;     ...
;                 for (int i = tid; i < 5 * D; i += NTHREADS) { const int r = i / D, k = i % D; const float v = r < 4 ? cvec[r * D + k] : c_ctx[k]; sc[i] = siluf(v); }
	v_fma_f32 v9, v44, s33, -v8
	v_rndne_f32_e32 v10, v8
	v_fmac_f32_e32 v9, 0xb2a5705f, v44
	v_sub_f32_e32 v8, v8, v10
	v_add_f32_e32 v8, v8, v9
	v_cvt_i32_f32_e32 v10, v10
	v_exp_f32_e32 v8, v8
	v_cmp_nlt_f32_e32 vcc, s36, v44
	v_ldexp_f32 v8, v8, v10
	s_nop 0
	v_cndmask_b32_e32 v8, 0, v8, vcc
	v_cmp_ngt_f32_e32 vcc, s37, v44
	s_nop 1
	v_cndmask_b32_e32 v8, v7, v8, vcc
	v_add_f32_e32 v8, 1.0, v8
	v_div_scale_f32 v9, s[34:35], v8, v8, v44
	v_rcp_f32_e32 v10, v9
	v_div_scale_f32 v11, vcc, v44, v8, v44
	v_fma_f32 v12, -v9, v10, 1.0
	v_fmac_f32_e32 v10, v12, v10
	v_mul_f32_e32 v12, v11, v10
	v_fma_f32 v13, -v9, v12, v11
	v_fmac_f32_e32 v12, v13, v10
	v_fma_f32 v9, -v9, v12, v11
	v_div_fmas_f32 v9, v9, v10, v12
	v_div_fixup_f32 v44, v9, v8, v44
	ds_write_b32 v194, v44 offset:8192
	v_mul_f32_e32 v8, 0xbfb8aa3b, v45
	v_fma_f32 v9, v45, s33, -v8
	v_rndne_f32_e32 v10, v8
	v_fmac_f32_e32 v9, 0xb2a5705f, v45
	v_sub_f32_e32 v8, v8, v10
	v_add_f32_e32 v8, v8, v9
	v_cvt_i32_f32_e32 v10, v10
	v_exp_f32_e32 v8, v8
	v_cmp_nlt_f32_e32 vcc, s36, v45
	v_ldexp_f32 v8, v8, v10
	s_nop 0
	v_cndmask_b32_e32 v8, 0, v8, vcc
	v_cmp_ngt_f32_e32 vcc, s37, v45
	s_nop 1
	v_cndmask_b32_e32 v8, v7, v8, vcc
	v_add_f32_e32 v8, 1.0, v8
	v_div_scale_f32 v9, s[34:35], v8, v8, v45
	v_rcp_f32_e32 v10, v9
	v_div_scale_f32 v11, vcc, v45, v8, v45
	v_fma_f32 v12, -v9, v10, 1.0
	v_fmac_f32_e32 v10, v12, v10
	v_mul_f32_e32 v12, v11, v10
	v_fma_f32 v13, -v9, v12, v11
	v_fmac_f32_e32 v12, v13, v10
	v_fma_f32 v9, -v9, v12, v11
	v_div_fmas_f32 v9, v9, v10, v12
	v_div_fixup_f32 v45, v9, v8, v45
	ds_write_b32 v194, v45 offset:10240
	v_mul_f32_e32 v8, 0xbfb8aa3b, v46
	v_fma_f32 v9, v46, s33, -v8
	v_rndne_f32_e32 v10, v8
	v_fmac_f32_e32 v9, 0xb2a5705f, v46
	v_sub_f32_e32 v8, v8, v10
	v_add_f32_e32 v8, v8, v9
	v_cvt_i32_f32_e32 v10, v10
	v_exp_f32_e32 v8, v8
	v_cmp_nlt_f32_e32 vcc, s36, v46
	v_ldexp_f32 v8, v8, v10
	s_nop 0
	v_cndmask_b32_e32 v8, 0, v8, vcc
	v_cmp_ngt_f32_e32 vcc, s37, v46
	s_nop 1
	v_cndmask_b32_e32 v8, v7, v8, vcc
	v_add_f32_e32 v8, 1.0, v8
	v_div_scale_f32 v9, s[34:35], v8, v8, v46
	v_rcp_f32_e32 v10, v9
	v_div_scale_f32 v11, vcc, v46, v8, v46
	v_fma_f32 v12, -v9, v10, 1.0
	v_fmac_f32_e32 v10, v12, v10
	v_mul_f32_e32 v12, v11, v10
	v_fma_f32 v13, -v9, v12, v11
	v_fmac_f32_e32 v12, v13, v10
	v_fma_f32 v9, -v9, v12, v11
	v_div_fmas_f32 v9, v9, v10, v12
	v_div_fixup_f32 v46, v9, v8, v46
	ds_write_b32 v194, v46 offset:12288
	v_mul_f32_e32 v8, 0xbfb8aa3b, v47
	v_fma_f32 v9, v47, s33, -v8
	v_rndne_f32_e32 v10, v8
	v_fmac_f32_e32 v9, 0xb2a5705f, v47
	v_sub_f32_e32 v8, v8, v10
	v_add_f32_e32 v8, v8, v9
	v_cvt_i32_f32_e32 v10, v10
	v_exp_f32_e32 v8, v8
	v_cmp_nlt_f32_e32 vcc, s36, v47
	v_ldexp_f32 v8, v8, v10
	s_nop 0
	v_cndmask_b32_e32 v8, 0, v8, vcc
	v_cmp_ngt_f32_e32 vcc, s37, v47
	s_nop 1
	v_cndmask_b32_e32 v8, v7, v8, vcc
	v_add_f32_e32 v8, 1.0, v8
	v_div_scale_f32 v9, s[34:35], v8, v8, v47
	v_rcp_f32_e32 v10, v9
	v_div_scale_f32 v11, vcc, v47, v8, v47
	v_fma_f32 v12, -v9, v10, 1.0
	v_fmac_f32_e32 v10, v12, v10
	v_mul_f32_e32 v12, v11, v10
	v_fma_f32 v13, -v9, v12, v11
	v_fmac_f32_e32 v12, v13, v10
	v_fma_f32 v9, -v9, v12, v11
	v_div_fmas_f32 v9, v9, v10, v12
	v_div_fixup_f32 v47, v9, v8, v47
	ds_write_b32 v194, v47 offset:14336
	v_mul_f32_e32 v8, 0xbfb8aa3b, v48
	v_fma_f32 v9, v48, s33, -v8
	v_rndne_f32_e32 v10, v8
	v_fmac_f32_e32 v9, 0xb2a5705f, v48
	v_sub_f32_e32 v8, v8, v10
	v_add_f32_e32 v8, v8, v9
	v_cvt_i32_f32_e32 v10, v10
	v_exp_f32_e32 v8, v8
	v_cmp_nlt_f32_e32 vcc, s36, v48
	v_ldexp_f32 v8, v8, v10
	s_nop 0
	v_cndmask_b32_e32 v8, 0, v8, vcc
	v_cmp_ngt_f32_e32 vcc, s37, v48
	s_nop 1
	v_cndmask_b32_e32 v8, v7, v8, vcc
	v_add_f32_e32 v8, 1.0, v8
	v_div_scale_f32 v9, s[34:35], v8, v8, v48
	v_rcp_f32_e32 v10, v9
	v_div_scale_f32 v11, vcc, v48, v8, v48
	v_fma_f32 v12, -v9, v10, 1.0
	v_fmac_f32_e32 v10, v12, v10
	v_mul_f32_e32 v12, v11, v10
	v_fma_f32 v13, -v9, v12, v11
	v_fmac_f32_e32 v12, v13, v10
	v_fma_f32 v9, -v9, v12, v11
	v_div_fmas_f32 v9, v9, v10, v12
	v_div_fixup_f32 v48, v9, v8, v48
	ds_write_b32 v194, v48 offset:16384
	v_mul_f32_e32 v8, 0xbfb8aa3b, v49
	v_fma_f32 v9, v49, s33, -v8
	v_rndne_f32_e32 v10, v8
	v_fmac_f32_e32 v9, 0xb2a5705f, v49
	v_sub_f32_e32 v8, v8, v10
	v_add_f32_e32 v8, v8, v9
	v_cvt_i32_f32_e32 v10, v10
	v_exp_f32_e32 v8, v8
	v_cmp_nlt_f32_e32 vcc, s36, v49
	v_ldexp_f32 v8, v8, v10
	s_nop 0
	v_cndmask_b32_e32 v8, 0, v8, vcc
	v_cmp_ngt_f32_e32 vcc, s37, v49
	s_nop 1
	v_cndmask_b32_e32 v8, v7, v8, vcc
	v_add_f32_e32 v8, 1.0, v8
	v_div_scale_f32 v9, s[34:35], v8, v8, v49
	v_rcp_f32_e32 v10, v9
	v_div_scale_f32 v11, vcc, v49, v8, v49
	v_fma_f32 v12, -v9, v10, 1.0
	v_fmac_f32_e32 v10, v12, v10
	v_mul_f32_e32 v12, v11, v10
	v_fma_f32 v13, -v9, v12, v11
	v_fmac_f32_e32 v12, v13, v10
	v_fma_f32 v9, -v9, v12, v11
	v_div_fmas_f32 v9, v9, v10, v12
	v_div_fixup_f32 v49, v9, v8, v49
	ds_write_b32 v194, v49 offset:18432
	v_mul_f32_e32 v8, 0xbfb8aa3b, v50
	v_fma_f32 v9, v50, s33, -v8
	v_rndne_f32_e32 v10, v8
	v_fmac_f32_e32 v9, 0xb2a5705f, v50
	v_sub_f32_e32 v8, v8, v10
	v_add_f32_e32 v8, v8, v9
	v_cvt_i32_f32_e32 v10, v10
	v_exp_f32_e32 v8, v8
	v_cmp_nlt_f32_e32 vcc, s36, v50
	v_ldexp_f32 v8, v8, v10
	s_nop 0
	v_cndmask_b32_e32 v8, 0, v8, vcc
	v_cmp_ngt_f32_e32 vcc, s37, v50
	s_nop 1
	v_cndmask_b32_e32 v8, v7, v8, vcc
	v_add_f32_e32 v8, 1.0, v8
	v_div_scale_f32 v9, s[34:35], v8, v8, v50
	v_rcp_f32_e32 v10, v9
	v_div_scale_f32 v11, vcc, v50, v8, v50
	v_fma_f32 v12, -v9, v10, 1.0
	v_fmac_f32_e32 v10, v12, v10
	v_mul_f32_e32 v12, v11, v10
	v_fma_f32 v13, -v9, v12, v11
	v_fmac_f32_e32 v12, v13, v10
	v_fma_f32 v9, -v9, v12, v11
	v_div_fmas_f32 v9, v9, v10, v12
; __device__ __forceinline__ float siluf(float x) { return x / (1.0f + expf(-x)); }
; __global__ void __launch_bounds__(NTHREADS, 2) fwd(Args args) {
;     ...
;                 for (int i = tid; i < 5 * D; i += NTHREADS) { const int r = i / D, k = i % D; const float v = r < 4 ? cvec[r * D + k] : c_ctx[k]; sc[i] = siluf(v); }
	v_div_fixup_f32 v50, v9, v8, v50
	ds_write_b32 v194, v50 offset:20480
	v_mul_f32_e32 v8, 0xbfb8aa3b, v51
	v_fma_f32 v9, v51, s33, -v8
	v_rndne_f32_e32 v10, v8
	v_fmac_f32_e32 v9, 0xb2a5705f, v51
	v_sub_f32_e32 v8, v8, v10
	v_add_f32_e32 v8, v8, v9
	v_cvt_i32_f32_e32 v10, v10
	v_exp_f32_e32 v8, v8
	v_cmp_nlt_f32_e32 vcc, s36, v51
	v_ldexp_f32 v8, v8, v10
	s_nop 0
	v_cndmask_b32_e32 v8, 0, v8, vcc
	v_cmp_ngt_f32_e32 vcc, s37, v51
	s_nop 1
	v_cndmask_b32_e32 v8, v7, v8, vcc
	v_add_f32_e32 v8, 1.0, v8
	v_div_scale_f32 v9, s[34:35], v8, v8, v51
	v_rcp_f32_e32 v10, v9
	v_div_scale_f32 v11, vcc, v51, v8, v51
	v_fma_f32 v12, -v9, v10, 1.0
	v_fmac_f32_e32 v10, v12, v10
	v_mul_f32_e32 v12, v11, v10
	v_fma_f32 v13, -v9, v12, v11
	v_fmac_f32_e32 v12, v13, v10
	v_fma_f32 v9, -v9, v12, v11
	v_div_fmas_f32 v9, v9, v10, v12
	v_div_fixup_f32 v51, v9, v8, v51
	ds_write_b32 v194, v51 offset:22528
	v_mul_f32_e32 v8, 0xbfb8aa3b, v52
	v_fma_f32 v9, v52, s33, -v8
	v_rndne_f32_e32 v10, v8
	v_fmac_f32_e32 v9, 0xb2a5705f, v52
	v_sub_f32_e32 v8, v8, v10
	v_add_f32_e32 v8, v8, v9
	v_cvt_i32_f32_e32 v10, v10
	v_exp_f32_e32 v8, v8
	v_cmp_nlt_f32_e32 vcc, s36, v52
	v_ldexp_f32 v8, v8, v10
	s_nop 0
	v_cndmask_b32_e32 v8, 0, v8, vcc
	v_cmp_ngt_f32_e32 vcc, s37, v52
	s_nop 1
	v_cndmask_b32_e32 v8, v7, v8, vcc
	v_add_f32_e32 v8, 1.0, v8
	v_div_scale_f32 v9, s[34:35], v8, v8, v52
	v_rcp_f32_e32 v10, v9
	v_div_scale_f32 v11, vcc, v52, v8, v52
	v_fma_f32 v12, -v9, v10, 1.0
	v_fmac_f32_e32 v10, v12, v10
	v_mul_f32_e32 v12, v11, v10
	v_fma_f32 v13, -v9, v12, v11
	v_fmac_f32_e32 v12, v13, v10
	v_fma_f32 v9, -v9, v12, v11
	v_div_fmas_f32 v9, v9, v10, v12
	v_div_fixup_f32 v52, v9, v8, v52
	ds_write_b32 v194, v52 offset:24576
	v_mul_f32_e32 v8, 0xbfb8aa3b, v53
	v_fma_f32 v9, v53, s33, -v8
	v_rndne_f32_e32 v10, v8
	v_fmac_f32_e32 v9, 0xb2a5705f, v53
	v_sub_f32_e32 v8, v8, v10
	v_add_f32_e32 v8, v8, v9
	v_cvt_i32_f32_e32 v10, v10
	v_exp_f32_e32 v8, v8
	v_cmp_nlt_f32_e32 vcc, s36, v53
	v_ldexp_f32 v8, v8, v10
	s_nop 0
	v_cndmask_b32_e32 v8, 0, v8, vcc
	v_cmp_ngt_f32_e32 vcc, s37, v53
	s_nop 1
	v_cndmask_b32_e32 v8, v7, v8, vcc
	v_add_f32_e32 v8, 1.0, v8
	v_div_scale_f32 v9, s[34:35], v8, v8, v53
	v_rcp_f32_e32 v10, v9
	v_div_scale_f32 v11, vcc, v53, v8, v53
	v_fma_f32 v12, -v9, v10, 1.0
	v_fmac_f32_e32 v10, v12, v10
	v_mul_f32_e32 v12, v11, v10
	v_fma_f32 v13, -v9, v12, v11
	v_fmac_f32_e32 v12, v13, v10
	v_fma_f32 v9, -v9, v12, v11
	v_div_fmas_f32 v9, v9, v10, v12
	v_div_fixup_f32 v53, v9, v8, v53
	ds_write_b32 v194, v53 offset:26624
	v_mul_f32_e32 v8, 0xbfb8aa3b, v54
	v_fma_f32 v9, v54, s33, -v8
	v_rndne_f32_e32 v10, v8
	v_fmac_f32_e32 v9, 0xb2a5705f, v54
	v_sub_f32_e32 v8, v8, v10
	v_add_f32_e32 v8, v8, v9
	v_cvt_i32_f32_e32 v10, v10
	v_exp_f32_e32 v8, v8
	v_cmp_nlt_f32_e32 vcc, s36, v54
	v_ldexp_f32 v8, v8, v10
	s_nop 0
	v_cndmask_b32_e32 v8, 0, v8, vcc
	v_cmp_ngt_f32_e32 vcc, s37, v54
	s_nop 1
	v_cndmask_b32_e32 v8, v7, v8, vcc
	v_add_f32_e32 v8, 1.0, v8
	v_div_scale_f32 v9, s[34:35], v8, v8, v54
	v_rcp_f32_e32 v10, v9
	v_div_scale_f32 v11, vcc, v54, v8, v54
	v_fma_f32 v12, -v9, v10, 1.0
	v_fmac_f32_e32 v10, v12, v10
	v_mul_f32_e32 v12, v11, v10
	v_fma_f32 v13, -v9, v12, v11
	v_fmac_f32_e32 v12, v13, v10
	v_fma_f32 v9, -v9, v12, v11
	v_div_fmas_f32 v9, v9, v10, v12
	v_div_fixup_f32 v54, v9, v8, v54
	ds_write_b32 v194, v54 offset:28672
	v_mul_f32_e32 v8, 0xbfb8aa3b, v55
	v_fma_f32 v9, v55, s33, -v8
	v_rndne_f32_e32 v10, v8
	v_fmac_f32_e32 v9, 0xb2a5705f, v55
	v_sub_f32_e32 v8, v8, v10
	v_add_f32_e32 v8, v8, v9
	v_cvt_i32_f32_e32 v10, v10
	v_exp_f32_e32 v8, v8
	v_cmp_nlt_f32_e32 vcc, s36, v55
	v_ldexp_f32 v8, v8, v10
	s_nop 0
	v_cndmask_b32_e32 v8, 0, v8, vcc
	v_cmp_ngt_f32_e32 vcc, s37, v55
	s_nop 1
	v_cndmask_b32_e32 v8, v7, v8, vcc
	v_add_f32_e32 v8, 1.0, v8
	v_div_scale_f32 v9, s[34:35], v8, v8, v55
	v_rcp_f32_e32 v10, v9
	v_div_scale_f32 v11, vcc, v55, v8, v55
	v_fma_f32 v12, -v9, v10, 1.0
	v_fmac_f32_e32 v10, v12, v10
	v_mul_f32_e32 v12, v11, v10
	v_fma_f32 v13, -v9, v12, v11
	v_fmac_f32_e32 v12, v13, v10
	v_fma_f32 v9, -v9, v12, v11
	v_div_fmas_f32 v9, v9, v10, v12
	v_div_fixup_f32 v55, v9, v8, v55
	ds_write_b32 v194, v55 offset:30720
; #define LBAR() do { asm volatile("s_waitcnt lgkmcnt(0)" ::: "memory"); __builtin_amdgcn_s_barrier(); asm volatile("" ::: "memory"); } while (0)
; __device__ __forceinline__ float siluf(float x) { return x / (1.0f + expf(-x)); }
; __global__ void __launch_bounds__(NTHREADS, 2) fwd(Args args) {
;     ...
;                 for (int i = tid; i < 5 * D; i += NTHREADS) { const int r = i / D, k = i % D; const float v = r < 4 ? cvec[r * D + k] : c_ctx[k]; sc[i] = siluf(v); }
;                 LBAR();
;             }
;             for (int u = bid; u < 192; u += G) {
;                 const int cg = tid & 15, kg = tid >> 4, n0 = u * 64 + cg * 4;
;                 float acc[5][4];
; #pragma unroll
;                 for (int r = 0; r < 5; ++r)
; #pragma unroll
;                     for (int j = 0; j < 4; ++j) acc[r][j] = 0.f;
; #pragma unroll 16
;                 for (int kk = 0; kk < 64; ++kk) { const int k = kg * 64 + kk; const f32x4 w = *(const f32x4*)(w_ada + (size_t)k * (6 * D) + n0);
	v_mul_f32_e32 v8, 0xbfb8aa3b, v56
	v_fma_f32 v9, v56, s33, -v8
	v_rndne_f32_e32 v10, v8
	v_fmac_f32_e32 v9, 0xb2a5705f, v56
	v_sub_f32_e32 v8, v8, v10
	v_add_f32_e32 v8, v8, v9
	v_cvt_i32_f32_e32 v10, v10
	v_exp_f32_e32 v8, v8
	v_cmp_nlt_f32_e32 vcc, s36, v56
	v_ldexp_f32 v8, v8, v10
	s_nop 0
	v_cndmask_b32_e32 v8, 0, v8, vcc
	v_cmp_ngt_f32_e32 vcc, s37, v56
	s_nop 1
	v_cndmask_b32_e32 v8, v7, v8, vcc
	v_add_f32_e32 v8, 1.0, v8
	v_div_scale_f32 v9, s[34:35], v8, v8, v56
	v_rcp_f32_e32 v10, v9
	v_div_scale_f32 v11, vcc, v56, v8, v56
	v_fma_f32 v12, -v9, v10, 1.0
	v_fmac_f32_e32 v10, v12, v10
	v_mul_f32_e32 v12, v11, v10
	v_fma_f32 v13, -v9, v12, v11
	v_fmac_f32_e32 v12, v13, v10
	v_fma_f32 v9, -v9, v12, v11
	v_div_fmas_f32 v9, v9, v10, v12
	v_div_fixup_f32 v56, v9, v8, v56
	ds_write_b32 v194, v56 offset:32768
	v_mul_f32_e32 v8, 0xbfb8aa3b, v57
	v_fma_f32 v9, v57, s33, -v8
	v_rndne_f32_e32 v10, v8
	v_fmac_f32_e32 v9, 0xb2a5705f, v57
	v_sub_f32_e32 v8, v8, v10
	v_add_f32_e32 v8, v8, v9
	v_cvt_i32_f32_e32 v10, v10
	v_exp_f32_e32 v8, v8
	v_cmp_nlt_f32_e32 vcc, s36, v57
	v_ldexp_f32 v8, v8, v10
	s_nop 0
	v_cndmask_b32_e32 v8, 0, v8, vcc
	v_cmp_ngt_f32_e32 vcc, s37, v57
	s_nop 1
	v_cndmask_b32_e32 v8, v7, v8, vcc
	v_add_f32_e32 v8, 1.0, v8
	v_div_scale_f32 v9, s[34:35], v8, v8, v57
	v_rcp_f32_e32 v10, v9
	v_div_scale_f32 v11, vcc, v57, v8, v57
	v_fma_f32 v12, -v9, v10, 1.0
	v_fmac_f32_e32 v10, v12, v10
	v_mul_f32_e32 v12, v11, v10
	v_fma_f32 v13, -v9, v12, v11
	v_fmac_f32_e32 v12, v13, v10
	v_fma_f32 v9, -v9, v12, v11
	v_div_fmas_f32 v9, v9, v10, v12
	v_div_fixup_f32 v57, v9, v8, v57
	ds_write_b32 v194, v57 offset:34816
	v_mul_f32_e32 v8, 0xbfb8aa3b, v58
	v_fma_f32 v9, v58, s33, -v8
	v_rndne_f32_e32 v10, v8
	v_fmac_f32_e32 v9, 0xb2a5705f, v58
	v_sub_f32_e32 v8, v8, v10
	v_add_f32_e32 v8, v8, v9
	v_cvt_i32_f32_e32 v10, v10
	v_exp_f32_e32 v8, v8
	v_cmp_nlt_f32_e32 vcc, s36, v58
	v_ldexp_f32 v8, v8, v10
	s_nop 0
	v_cndmask_b32_e32 v8, 0, v8, vcc
	v_cmp_ngt_f32_e32 vcc, s37, v58
	s_nop 1
	v_cndmask_b32_e32 v8, v7, v8, vcc
	v_add_f32_e32 v8, 1.0, v8
	v_div_scale_f32 v9, s[34:35], v8, v8, v58
	v_rcp_f32_e32 v10, v9
	v_div_scale_f32 v11, vcc, v58, v8, v58
	v_fma_f32 v12, -v9, v10, 1.0
	v_fmac_f32_e32 v10, v12, v10
	v_mul_f32_e32 v12, v11, v10
	v_fma_f32 v13, -v9, v12, v11
	v_fmac_f32_e32 v12, v13, v10
	v_fma_f32 v9, -v9, v12, v11
	v_div_fmas_f32 v9, v9, v10, v12
	v_div_fixup_f32 v58, v9, v8, v58
	ds_write_b32 v194, v58 offset:36864
	v_mul_f32_e32 v8, 0xbfb8aa3b, v59
	v_fma_f32 v9, v59, s33, -v8
	v_rndne_f32_e32 v10, v8
	v_fmac_f32_e32 v9, 0xb2a5705f, v59
	v_sub_f32_e32 v8, v8, v10
	v_add_f32_e32 v8, v8, v9
	v_cvt_i32_f32_e32 v10, v10
	v_exp_f32_e32 v8, v8
	v_cmp_nlt_f32_e32 vcc, s36, v59
	v_ldexp_f32 v8, v8, v10
	s_nop 0
	v_cndmask_b32_e32 v8, 0, v8, vcc
	v_cmp_ngt_f32_e32 vcc, s37, v59
	s_nop 1
	v_cndmask_b32_e32 v8, v7, v8, vcc
	v_add_f32_e32 v8, 1.0, v8
	v_div_scale_f32 v9, s[34:35], v8, v8, v59
	v_rcp_f32_e32 v10, v9
	v_div_scale_f32 v11, vcc, v59, v8, v59
	v_fma_f32 v12, -v9, v10, 1.0
	v_fmac_f32_e32 v10, v12, v10
	v_mul_f32_e32 v12, v11, v10
	v_fma_f32 v13, -v9, v12, v11
	v_fmac_f32_e32 v12, v13, v10
	v_fma_f32 v9, -v9, v12, v11
	v_div_fmas_f32 v9, v9, v10, v12
	v_div_fixup_f32 v59, v9, v8, v59
	ds_write_b32 v194, v59 offset:38912
.LBB0_16:
	s_movk_i32 s2, 0x140
	v_mov_b32_e32 v2, s28
	v_mov_b32_e32 v3, s29
	v_lshrrev_b32_e32 v4, 4, v0
	v_cmp_gt_u32_e32 vcc, s2, v0
	s_mov_b32 s2, 0x300000
	v_lshrrev_b32_e32 v7, 6, v0
	v_mad_u64_u32 v[48:49], s[2:3], v4, s2, v[2:3]
	s_waitcnt lgkmcnt(0)
	s_barrier
	v_and_b32_e32 v5, 60, v194
	v_lshlrev_b32_e32 v8, 2, v220
	v_mul_u32_u24_e32 v1, 0x3000, v7
	v_lshlrev_b32_e32 v7, 8, v7
	v_readlane_b32 s2, v246, 10
	v_lshl_add_u32 v6, v5, 2, 0
	v_mul_u32_u24_e32 v9, 0x500, v4
	v_add3_u32 v71, 0, v8, v7
	v_readlane_b32 s3, v246, 11
	v_or_b32_e32 v1, v1, v220
	v_add_u32_e32 v72, 0xa000, v71
	v_lshl_or_b32 v50, s94, 6, v5
	s_lshl_b32 s2, s2, 6
	v_lshl_add_u32 v73, v4, 8, 0
	s_mov_b32 s3, 0x6c000
	s_mov_b32 s8, 0x78000
	s_mov_b32 s9, 0x84000
	s_mov_b32 s10, 0x90000
	s_mov_b32 s11, 0x9c000
	s_mov_b32 s12, 0xa8000
	s_mov_b32 s13, 0xb4000
	v_add_u32_e32 v74, v6, v9
	s_mov_b32 s18, s94
	s_branch .LBB0_18
